# F-copy of attn loop2: exp blocks rescheduled S1-first (no s_nop padding), hazard fix in general copy (s_nop 8)
# baseline (speedup 1.0000x reference)
.LBB4_7:
	v_exp_f32_e32 v215, v66
	s_nop 8
	v_fma_f32 v66, v82, s4, -v188
	v_exp_f32_e32 v216, v66
	v_exp_f32_e32 v217, v67
	v_fma_f32 v66, v83, s4, -v188
	v_exp_f32_e32 v214, v66
	v_exp_f32_e32 v219, v68
	v_fma_f32 v66, v84, s4, -v188
	v_exp_f32_e32 v220, v66
	ds_read_b128 v[98:101], v186 offset:18432
	ds_read_b128 v[162:165], v186 offset:18464
	ds_read_b128 v[194:197], v186 offset:27648
	ds_read_b128 v[198:201], v186 offset:27680
	ds_read_b128 v[202:205], v186 offset:18496
	ds_read_b128 v[206:209], v186 offset:18528
	ds_read_b128 v[210:213], v186 offset:27712
	ds_read_b128 v[166:169], v186 offset:27744
	v_exp_f32_e32 v221, v69
	v_fma_f32 v66, v85, s4, -v188
	v_exp_f32_e32 v218, v66
	s_waitcnt lgkmcnt(7)
	v_mfma_f32_32x32x16_f16 v[98:113], v[98:101], v[114:117], v[240:255]
	v_exp_f32_e32 v223, v70
	v_fma_f32 v66, v86, s4, -v188
	v_exp_f32_e32 v70, v66
	v_exp_f32_e32 v71, v71
	v_fma_f32 v66, v87, s4, -v188
	v_exp_f32_e32 v222, v66
	v_exp_f32_e32 v225, v72
	v_fma_f32 v66, v88, s4, -v188
	v_exp_f32_e32 v226, v66
	v_exp_f32_e32 v227, v73
	v_fma_f32 v66, v89, s4, -v188
	v_exp_f32_e32 v224, v66
	s_waitcnt lgkmcnt(6)
	v_mfma_f32_32x32x16_f16 v[98:113], v[162:165], v[118:121], v[98:113]
	v_exp_f32_e32 v229, v74
	v_fma_f32 v66, v90, s4, -v188
	v_exp_f32_e32 v230, v66
	v_exp_f32_e32 v231, v75
	v_fma_f32 v66, v91, s4, -v188
	v_exp_f32_e32 v228, v66
	v_exp_f32_e32 v233, v76
	v_fma_f32 v66, v92, s4, -v188
	v_exp_f32_e32 v234, v66
	v_exp_f32_e32 v235, v77
	v_fma_f32 v66, v93, s4, -v188
	v_exp_f32_e32 v232, v66
	s_waitcnt lgkmcnt(3)
	v_mfma_f32_32x32x16_f16 v[98:113], v[202:205], v[122:125], v[98:113]
	v_exp_f32_e32 v237, v78
	v_fma_f32 v66, v94, s4, -v188
	v_exp_f32_e32 v162, v66
	v_exp_f32_e32 v163, v79
	v_fma_f32 v66, v95, s4, -v188
	v_exp_f32_e32 v236, v66
	v_exp_f32_e32 v165, v80
	v_fma_f32 v66, v96, s4, -v188
	v_exp_f32_e32 v202, v66
	v_exp_f32_e32 v203, v81
	v_fma_f32 v66, v97, s4, -v188
	v_exp_f32_e32 v193, v66
	s_waitcnt lgkmcnt(2)
	v_mfma_f32_32x32x16_f16 v[98:113], v[206:209], v[126:129], v[98:113]
	s_waitcnt vmcnt(3)
	ds_write_b128 v185, v[146:149]
	s_waitcnt vmcnt(2)
	ds_write_b128 v185, v[150:153] offset:9216
	s_waitcnt vmcnt(1)
	ds_write_b128 v185, v[154:157] offset:55296
	s_waitcnt vmcnt(0)
	ds_write_b128 v185, v[158:161] offset:64512
	v_fma_f32 v150, v176, v216, v215
	v_fma_f32 v151, v176, v214, v217
	ds_read_b128 v[66:69], v189
	ds_read_b128 v[88:91], v189 offset:1152
	v_fma_f32 v152, v176, v220, v219
	v_fma_f32 v153, v176, v218, v221
	ds_read_b128 v[92:95], v189 offset:2304
	ds_read_b128 v[146:149], v189 offset:3456
	v_fma_f32 v154, v176, v70, v223
	v_fma_f32 v155, v176, v222, v71
	ds_write_b128 v190, v[150:153]
	v_fma_f32 v156, v176, v226, v225
	v_fma_f32 v157, v176, v224, v227
	ds_write_b128 v190, v[154:157] offset:16
	v_fma_f32 v158, v176, v230, v229
	v_fma_f32 v159, v176, v228, v231
	v_cvt_pk_f16_f32 v157, v156, v157
	v_fma_f32 v160, v176, v234, v233
	v_fma_f32 v161, v176, v232, v235
	ds_write_b128 v190, v[158:161] offset:64
	v_fma_f32 v162, v176, v162, v237
	v_fma_f32 v163, v176, v236, v163
	v_cvt_pk_f16_f32 v156, v154, v155
	v_fma_f32 v164, v176, v202, v165
	v_fma_f32 v165, v176, v193, v203
	ds_write_b128 v190, v[162:165] offset:80
	v_cvt_pk_f16_f32 v155, v152, v153
	v_cvt_pk_f16_f32 v154, v150, v151
	ds_read_b128 v[150:153], v191 offset:36864
	s_cmp_eq_u32 s19, 0
	s_cselect_b64 vcc, -1, 0
	s_add_i32 s20, s16, s1
	v_mfma_f32_32x32x16_f16 v[72:87], v[194:197], v[130:133], 0
	ds_read_b128 v[194:197], v191 offset:36896
	s_add_i32 s2, s20, 0x7c0
	s_and_b32 s2, s2, 0x7c0
	s_lshl_b32 s2, s2, 2
	v_lshl_add_u64 v[70:71], v[174:175], 0, s[2:3]
	v_cndmask_b32_e32 v71, v71, v179, vcc
	v_cndmask_b32_e32 v70, v70, v178, vcc
	s_waitcnt lgkmcnt(1)
	v_mfma_f32_32x32x16_f16 v[50:65], v[154:157], v[150:153], v[50:65]
	ds_read_b128 v[150:153], v191 offset:41472
	global_store_dwordx4 v[70:71], v[66:69], off nt
	ds_read_b128 v[66:69], v191 offset:41504
	v_cvt_pk_f16_f32 v165, v164, v165
	v_cvt_pk_f16_f32 v164, v162, v163
	v_cvt_pk_f16_f32 v163, v160, v161
	v_cvt_pk_f16_f32 v162, v158, v159
	s_waitcnt lgkmcnt(1)
	v_mfma_f32_32x32x16_f16 v[34:49], v[154:157], v[150:153], v[34:49]
	v_add_co_u32_e32 v96, vcc, s5, v70
	s_min_u32 s2, s19, 28
	s_nop 0
	v_addc_co_u32_e32 v97, vcc, 0, v71, vcc
	global_store_dwordx4 v[96:97], v[88:91], off nt
	s_add_i32 s21, s17, s2
	s_waitcnt lgkmcnt(0)
	v_mfma_f32_32x32x16_f16 v[34:49], v[162:165], v[66:69], v[34:49]
	ds_read_b128 v[66:69], v191 offset:46080
	v_add_co_u32_e32 v88, vcc, s13, v70
	s_lshl_b32 s2, s21, 13
	s_nop 0
	v_addc_co_u32_e32 v89, vcc, 0, v71, vcc
	global_store_dwordx4 v[88:89], v[92:95], off nt
	ds_read_b128 v[88:91], v191 offset:46112
	s_waitcnt lgkmcnt(1)
	v_mfma_f32_32x32x16_f16 v[18:33], v[154:157], v[66:69], v[18:33]
	v_add_co_u32_e32 v70, vcc, s14, v70
	s_and_b32 s2, s2, 0x3e000
	s_nop 0
	v_addc_co_u32_e32 v71, vcc, 0, v71, vcc
	v_lshl_add_u64 v[66:67], v[170:171], 0, s[2:3]
	v_add_co_u32_e32 v68, vcc, s15, v66
	global_store_dwordx4 v[70:71], v[146:149], off nt
	s_nop 0
	v_addc_co_u32_e32 v69, vcc, 0, v67, vcc
	s_waitcnt lgkmcnt(0)
	v_mfma_f32_32x32x16_f16 v[18:33], v[162:165], v[88:91], v[18:33]
	global_load_dwordx4 v[88:91], v[66:67], off
	global_load_dwordx4 v[92:95], v[68:69], off
	ds_read_b128 v[66:69], v191 offset:50688
	ds_read_b128 v[146:149], v191 offset:50720
	s_min_u32 s2, s19, 29
	s_add_i32 s2, s0, s2
	s_lshl_b32 s2, s2, 7
	s_and_b32 s2, s2, 0xf80
	s_waitcnt lgkmcnt(1)
	v_mfma_f32_32x32x16_f16 v[2:17], v[154:157], v[66:69], v[2:17]
	v_lshl_add_u64 v[66:67], v[172:173], 0, s[2:3]
	v_add_co_u32_e32 v68, vcc, s10, v66
	s_nop 0
	v_addc_co_u32_e32 v69, vcc, 0, v67, vcc
	global_load_dwordx4 v[150:153], v[66:67], off
	global_load_dwordx4 v[154:157], v[68:69], off
	v_mfma_f32_32x32x16_f16 v[72:87], v[198:201], v[134:137], v[72:87]
	v_exp_f32_e32 v97, v98
	s_waitcnt lgkmcnt(0)
	s_barrier
	v_mfma_f32_32x32x16_f16 v[72:87], v[210:213], v[138:141], v[72:87]
	v_mfma_f32_32x32x16_f16 v[72:87], v[166:169], v[142:145], v[72:87]
	v_mfma_f32_32x32x16_f16 v[50:65], v[162:165], v[194:197], v[50:65]
	s_nop 10
	v_fma_f32 v70, v72, s4, -v188
	v_exp_f32_e32 v166, v70
	v_exp_f32_e32 v167, v99
	v_fma_f32 v70, v73, s4, -v188
	v_exp_f32_e32 v96, v70
	v_exp_f32_e32 v99, v100
	v_fma_f32 v70, v74, s4, -v188
	v_exp_f32_e32 v168, v70
	v_exp_f32_e32 v169, v101
	v_fma_f32 v70, v75, s4, -v188
	v_exp_f32_e32 v98, v70
	v_exp_f32_e32 v101, v102
	v_fma_f32 v70, v76, s4, -v188
	v_exp_f32_e32 v210, v70
	v_exp_f32_e32 v211, v103
	v_fma_f32 v70, v77, s4, -v188
	v_exp_f32_e32 v100, v70
	v_exp_f32_e32 v103, v104
	v_fma_f32 v70, v78, s4, -v188
	v_exp_f32_e32 v212, v70
	v_exp_f32_e32 v213, v105
	v_fma_f32 v70, v79, s4, -v188
	v_exp_f32_e32 v102, v70
	v_exp_f32_e32 v105, v106
	v_fma_f32 v70, v80, s4, -v188
	v_exp_f32_e32 v214, v70
	v_exp_f32_e32 v215, v107
	v_fma_f32 v70, v81, s4, -v188
	v_mfma_f32_32x32x16_f16 v[2:17], v[162:165], v[146:149], v[2:17]
	ds_read_b128 v[66:69], v186
	ds_read_b128 v[158:161], v186 offset:32
	ds_read_b128 v[194:197], v186 offset:9216
	ds_read_b128 v[198:201], v186 offset:9248
	ds_read_b128 v[202:205], v186 offset:64
	ds_read_b128 v[206:209], v186 offset:96
	ds_read_b128 v[146:149], v186 offset:9280
	ds_read_b128 v[162:165], v186 offset:9312
	v_exp_f32_e32 v104, v70
	v_exp_f32_e32 v107, v108
	v_fma_f32 v82, v82, s4, -v188
	v_exp_f32_e32 v216, v82
	s_waitcnt lgkmcnt(7)
	v_mfma_f32_32x32x16_f16 v[66:81], v[66:69], v[114:117], v[240:255]
	v_exp_f32_e32 v217, v109
	v_fma_f32 v82, v83, s4, -v188
	v_exp_f32_e32 v106, v82
	v_exp_f32_e32 v109, v110
	v_fma_f32 v82, v84, s4, -v188
	v_exp_f32_e32 v218, v82
	s_waitcnt lgkmcnt(6)
	v_mfma_f32_32x32x16_f16 v[66:81], v[158:161], v[118:121], v[66:81]
	v_exp_f32_e32 v219, v111
	v_fma_f32 v82, v85, s4, -v188
	v_exp_f32_e32 v108, v82
	v_exp_f32_e32 v111, v112
	v_fma_f32 v82, v86, s4, -v188
	s_waitcnt lgkmcnt(3)
	v_mfma_f32_32x32x16_f16 v[66:81], v[202:205], v[122:125], v[66:81]
	v_exp_f32_e32 v202, v82
	v_exp_f32_e32 v203, v113
	v_fma_f32 v82, v87, s4, -v188
	v_exp_f32_e32 v110, v82
	s_waitcnt lgkmcnt(2)
	v_mfma_f32_32x32x16_f16 v[66:81], v[206:209], v[126:129], v[66:81]
	s_waitcnt vmcnt(3)
	ds_write_b128 v185, v[88:91] offset:18432
	s_waitcnt vmcnt(2)
	ds_write_b128 v185, v[92:95] offset:27648
	s_waitcnt vmcnt(1)
	ds_write_b128 v185, v[150:153] offset:36864
	s_waitcnt vmcnt(0)
	ds_write_b128 v185, v[154:157] offset:46080
	v_fma_f32 v150, v176, v166, v97
	v_fma_f32 v151, v176, v96, v167
	v_mfma_f32_32x32x16_f16 v[82:97], v[194:197], v[130:133], 0
	v_fma_f32 v152, v176, v168, v99
	v_fma_f32 v153, v176, v98, v169
	v_fma_f32 v154, v176, v210, v101
	v_fma_f32 v155, v176, v100, v211
	v_fma_f32 v156, v176, v212, v103
	v_fma_f32 v157, v176, v102, v213
	v_fma_f32 v158, v176, v214, v105
	v_fma_f32 v159, v176, v104, v215
	v_fma_f32 v160, v176, v216, v107
	v_fma_f32 v161, v176, v106, v217
	v_fma_f32 v166, v176, v218, v109
	v_fma_f32 v167, v176, v108, v219
	v_fma_f32 v168, v176, v202, v111
	v_fma_f32 v169, v176, v110, v203
	ds_read_b128 v[98:101], v189
	ds_read_b128 v[102:105], v189 offset:1152
	ds_read_b128 v[106:109], v189 offset:2304
	ds_read_b128 v[110:113], v189 offset:3456
	ds_write_b128 v190, v[150:153]
	ds_write_b128 v190, v[154:157] offset:16
	ds_write_b128 v190, v[158:161] offset:64
	ds_write_b128 v190, v[166:169] offset:80
	v_cvt_pk_f16_f32 v157, v156, v157
	v_cvt_pk_f16_f32 v156, v154, v155
	v_cvt_pk_f16_f32 v155, v152, v153
	v_cvt_pk_f16_f32 v154, v150, v151
	ds_read_b128 v[150:153], v191 offset:55296
	ds_read_b128 v[194:197], v191 offset:55328
	v_mfma_f32_32x32x16_f16 v[82:97], v[198:201], v[134:137], v[82:97]
	s_and_b32 s2, s20, 0x7c0
	s_min_u32 s20, s19, 27
	s_lshl_b32 s2, s2, 2
	s_add_i32 s20, s18, s20
	v_lshl_add_u64 v[210:211], v[174:175], 0, s[2:3]
	s_lshl_b32 s2, s20, 13
	s_and_b32 s2, s2, 0x3e000
	s_waitcnt lgkmcnt(1)
	v_mfma_f32_32x32x16_f16 v[50:65], v[154:157], v[150:153], v[50:65]
	ds_read_b128 v[150:153], v191 offset:59904
	ds_read_b128 v[198:201], v191 offset:59936
	s_lshl_b32 s21, s21, 7
	v_cvt_pk_f16_f32 v169, v168, v169
	v_cvt_pk_f16_f32 v168, v166, v167
	v_cvt_pk_f16_f32 v166, v158, v159
	v_cvt_pk_f16_f32 v167, v160, v161
	s_addk_i32 s1, 0x80
	s_waitcnt lgkmcnt(1)
	v_mfma_f32_32x32x16_f16 v[34:49], v[154:157], v[150:153], v[34:49]
	ds_read_b128 v[150:153], v191 offset:64512
	ds_read_b128 v[202:205], v191 offset:64544
	s_waitcnt lgkmcnt(1)
	v_mfma_f32_32x32x16_f16 v[18:33], v[154:157], v[150:153], v[18:33]
	ds_read_b128 v[150:153], v192 offset:13824
	ds_read_b128 v[206:209], v192 offset:13856
	v_mfma_f32_32x32x16_f16 v[82:97], v[146:149], v[138:141], v[82:97]
	v_lshl_add_u64 v[146:147], v[170:171], 0, s[2:3]
	s_and_b32 s2, s21, 0xf80
	v_lshl_add_u64 v[158:159], v[172:173], 0, s[2:3]
	s_add_i32 s2, s19, 2
	s_cmp_lt_u32 s19, 30
	s_mov_b32 s19, s2
	s_waitcnt lgkmcnt(1)
	v_mfma_f32_32x32x16_f16 v[2:17], v[154:157], v[150:153], v[2:17]
	v_add_co_u32_e32 v150, vcc, s15, v146
	s_nop 1
	v_addc_co_u32_e32 v151, vcc, 0, v147, vcc
	global_load_dwordx4 v[146:149], v[146:147], off
	s_nop 0
	global_load_dwordx4 v[150:153], v[150:151], off
	s_nop 0
	global_load_dwordx4 v[154:157], v[158:159], off
	v_add_co_u32_e32 v158, vcc, s10, v158
	v_mfma_f32_32x32x16_f16 v[50:65], v[166:169], v[194:197], v[50:65]
	s_nop 0
	v_addc_co_u32_e32 v159, vcc, 0, v159, vcc
	global_load_dwordx4 v[158:161], v[158:159], off
	v_add_co_u32_e32 v194, vcc, s5, v210
	s_nop 1
	v_addc_co_u32_e32 v195, vcc, 0, v211, vcc
	v_mfma_f32_32x32x16_f16 v[34:49], v[166:169], v[198:201], v[34:49]
	v_add_co_u32_e32 v196, vcc, s13, v210
	s_nop 1
	v_addc_co_u32_e32 v197, vcc, 0, v211, vcc
	v_mfma_f32_32x32x16_f16 v[18:33], v[166:169], v[202:205], v[18:33]
	s_waitcnt lgkmcnt(0)
	v_mfma_f32_32x32x16_f16 v[2:17], v[166:169], v[206:209], v[2:17]
	v_add_co_u32_e32 v166, vcc, s14, v210
	s_nop 1
	v_addc_co_u32_e32 v167, vcc, 0, v211, vcc
	global_store_dwordx4 v[210:211], v[98:101], off nt
	global_store_dwordx4 v[194:195], v[102:105], off nt
	global_store_dwordx4 v[196:197], v[106:109], off nt
	global_store_dwordx4 v[166:167], v[110:113], off nt
	v_mfma_f32_32x32x16_f16 v[82:97], v[162:165], v[142:145], v[82:97]
	s_barrier
	s_cbranch_scc1 .LBB4_7
	s_branch .Ll2_post
	.p2alignl 6, 3212836864
	s_nop 0
	s_nop 0
	s_nop 0
	s_nop 0
.Ll2f_top:
	ds_read_b128 v[98:101], v186 offset:18432
	ds_read_b128 v[162:165], v186 offset:18464
	ds_read_b128 v[194:197], v186 offset:27648
	ds_read_b128 v[198:201], v186 offset:27680
	ds_read_b128 v[202:205], v186 offset:18496
	ds_read_b128 v[206:209], v186 offset:18528
	ds_read_b128 v[210:213], v186 offset:27712
	ds_read_b128 v[166:169], v186 offset:27744
	s_nop 0
	v_exp_f32_e32 v215, v66
	v_exp_f32_e32 v217, v67
	v_exp_f32_e32 v219, v68
	v_exp_f32_e32 v221, v69
	v_exp_f32_e32 v223, v70
	v_exp_f32_e32 v71, v71
	v_exp_f32_e32 v225, v72
	v_exp_f32_e32 v227, v73
	v_exp_f32_e32 v229, v74
	v_exp_f32_e32 v231, v75
	s_waitcnt lgkmcnt(7)
	v_mfma_f32_32x32x16_f16 v[98:113], v[98:101], v[114:117], v[240:255]
	v_exp_f32_e32 v216, v82
	v_exp_f32_e32 v214, v83
	v_exp_f32_e32 v220, v84
	v_exp_f32_e32 v218, v85
	v_exp_f32_e32 v70, v86
	v_exp_f32_e32 v222, v87
	v_exp_f32_e32 v226, v88
	v_exp_f32_e32 v224, v89
	s_waitcnt lgkmcnt(6)
	v_mfma_f32_32x32x16_f16 v[98:113], v[162:165], v[118:121], v[98:113]
	v_exp_f32_e32 v233, v76
	v_exp_f32_e32 v235, v77
	v_exp_f32_e32 v230, v90
	v_exp_f32_e32 v228, v91
	v_exp_f32_e32 v234, v92
	v_exp_f32_e32 v232, v93
	v_exp_f32_e32 v237, v78
	v_exp_f32_e32 v236, v95
	s_waitcnt lgkmcnt(3)
	v_mfma_f32_32x32x16_f16 v[98:113], v[202:205], v[122:125], v[98:113]
	v_exp_f32_e32 v162, v94
	v_exp_f32_e32 v163, v79
	v_exp_f32_e32 v165, v80
	v_exp_f32_e32 v202, v96
	v_exp_f32_e32 v203, v81
	v_exp_f32_e32 v193, v97
	s_waitcnt lgkmcnt(2)
	v_mfma_f32_32x32x16_f16 v[98:113], v[206:209], v[126:129], v[98:113]
	s_waitcnt vmcnt(3)
	ds_write_b128 v185, v[146:149]
	s_waitcnt vmcnt(2)
	ds_write_b128 v185, v[150:153] offset:9216
	s_waitcnt vmcnt(1)
	ds_write_b128 v185, v[154:157] offset:55296
	s_waitcnt vmcnt(0)
	ds_write_b128 v185, v[158:161] offset:64512
	v_fma_f32 v150, v176, v216, v215
	v_fma_f32 v151, v176, v214, v217
	ds_read_b128 v[66:69], v189
	ds_read_b128 v[88:91], v189 offset:1152
	v_fma_f32 v152, v176, v220, v219
	v_fma_f32 v153, v176, v218, v221
	ds_read_b128 v[92:95], v189 offset:2304
	ds_read_b128 v[146:149], v189 offset:3456
	v_fma_f32 v154, v176, v70, v223
	v_fma_f32 v155, v176, v222, v71
	ds_write_b128 v190, v[150:153]
	v_fma_f32 v156, v176, v226, v225
	v_fma_f32 v157, v176, v224, v227
	ds_write_b128 v190, v[154:157] offset:16
	v_fma_f32 v158, v176, v230, v229
	v_fma_f32 v159, v176, v228, v231
	v_cvt_pk_f16_f32 v157, v156, v157
	v_fma_f32 v160, v176, v234, v233
	v_fma_f32 v161, v176, v232, v235
	ds_write_b128 v190, v[158:161] offset:64
	v_fma_f32 v162, v176, v162, v237
	v_fma_f32 v163, v176, v236, v163
	v_cvt_pk_f16_f32 v156, v154, v155
	v_fma_f32 v164, v176, v202, v165
	v_fma_f32 v165, v176, v193, v203
	ds_write_b128 v190, v[162:165] offset:80
	v_cvt_pk_f16_f32 v155, v152, v153
	v_cvt_pk_f16_f32 v154, v150, v151
	ds_read_b128 v[150:153], v191 offset:36864
	s_cmp_eq_u32 s19, 0
	s_cselect_b64 vcc, -1, 0
	s_add_i32 s20, s16, s1
	v_mfma_f32_32x32x16_f16 v[72:87], v[194:197], v[130:133], 0
	ds_read_b128 v[194:197], v191 offset:36896
	s_add_i32 s2, s20, 0x7c0
	s_and_b32 s2, s2, 0x7c0
	s_lshl_b32 s2, s2, 2
	v_lshl_add_u64 v[70:71], v[174:175], 0, s[2:3]
	v_cndmask_b32_e32 v71, v71, v179, vcc
	v_cndmask_b32_e32 v70, v70, v178, vcc
	s_waitcnt lgkmcnt(1)
	v_mfma_f32_32x32x16_f16 v[50:65], v[154:157], v[150:153], v[50:65]
	ds_read_b128 v[150:153], v191 offset:41472
	global_store_dwordx4 v[70:71], v[66:69], off nt
	ds_read_b128 v[66:69], v191 offset:41504
	v_cvt_pk_f16_f32 v165, v164, v165
	v_cvt_pk_f16_f32 v164, v162, v163
	v_cvt_pk_f16_f32 v163, v160, v161
	v_cvt_pk_f16_f32 v162, v158, v159
	s_waitcnt lgkmcnt(1)
	v_mfma_f32_32x32x16_f16 v[34:49], v[154:157], v[150:153], v[34:49]
	v_add_co_u32_e32 v96, vcc, s5, v70
	s_min_u32 s2, s19, 28
	s_nop 0
	v_addc_co_u32_e32 v97, vcc, 0, v71, vcc
	global_store_dwordx4 v[96:97], v[88:91], off nt
	s_add_i32 s21, s17, s2
	s_waitcnt lgkmcnt(0)
	v_mfma_f32_32x32x16_f16 v[34:49], v[162:165], v[66:69], v[34:49]
	ds_read_b128 v[66:69], v191 offset:46080
	v_add_co_u32_e32 v88, vcc, s13, v70
	s_lshl_b32 s2, s21, 13
	s_nop 0
	v_addc_co_u32_e32 v89, vcc, 0, v71, vcc
	global_store_dwordx4 v[88:89], v[92:95], off nt
	ds_read_b128 v[88:91], v191 offset:46112
	s_waitcnt lgkmcnt(1)
	v_mfma_f32_32x32x16_f16 v[18:33], v[154:157], v[66:69], v[18:33]
	v_add_co_u32_e32 v70, vcc, s14, v70
	s_and_b32 s2, s2, 0x3e000
	s_nop 0
	v_addc_co_u32_e32 v71, vcc, 0, v71, vcc
	v_lshl_add_u64 v[66:67], v[170:171], 0, s[2:3]
	v_add_co_u32_e32 v68, vcc, s15, v66
	global_store_dwordx4 v[70:71], v[146:149], off nt
	s_nop 0
	v_addc_co_u32_e32 v69, vcc, 0, v67, vcc
	s_waitcnt lgkmcnt(0)
	v_mfma_f32_32x32x16_f16 v[18:33], v[162:165], v[88:91], v[18:33]
	global_load_dwordx4 v[88:91], v[66:67], off
	global_load_dwordx4 v[92:95], v[68:69], off
	ds_read_b128 v[66:69], v191 offset:50688
	ds_read_b128 v[146:149], v191 offset:50720
	s_min_u32 s2, s19, 29
	s_add_i32 s2, s0, s2
	s_lshl_b32 s2, s2, 7
	s_and_b32 s2, s2, 0xf80
	s_waitcnt lgkmcnt(1)
	v_mfma_f32_32x32x16_f16 v[2:17], v[154:157], v[66:69], v[2:17]
	v_lshl_add_u64 v[66:67], v[172:173], 0, s[2:3]
	v_add_co_u32_e32 v68, vcc, s10, v66
	s_nop 0
	v_addc_co_u32_e32 v69, vcc, 0, v67, vcc
	global_load_dwordx4 v[150:153], v[66:67], off
	global_load_dwordx4 v[154:157], v[68:69], off
	v_mfma_f32_32x32x16_f16 v[72:87], v[198:201], v[134:137], v[72:87]
	v_exp_f32_e32 v97, v98
	s_waitcnt lgkmcnt(0)
	s_barrier
	v_mfma_f32_32x32x16_f16 v[72:87], v[210:213], v[138:141], v[72:87]
	v_mfma_f32_32x32x16_f16 v[72:87], v[166:169], v[142:145], v[72:87]
	v_mfma_f32_32x32x16_f16 v[50:65], v[162:165], v[194:197], v[50:65]
	s_nop 0
	ds_read_b128 v[66:69], v186
	ds_read_b128 v[158:161], v186 offset:32
	ds_read_b128 v[194:197], v186 offset:9216
	ds_read_b128 v[198:201], v186 offset:9248
	ds_read_b128 v[202:205], v186 offset:64
	ds_read_b128 v[206:209], v186 offset:96
	v_exp_f32_e32 v167, v99
	v_exp_f32_e32 v99, v100
	v_exp_f32_e32 v169, v101
	v_exp_f32_e32 v101, v102
	v_mfma_f32_32x32x16_f16 v[2:17], v[162:165], v[146:149], v[2:17]
	ds_read_b128 v[146:149], v186 offset:9280
	ds_read_b128 v[162:165], v186 offset:9312
	v_exp_f32_e32 v211, v103
	v_exp_f32_e32 v103, v104
	v_exp_f32_e32 v213, v105
	v_exp_f32_e32 v105, v106
	v_exp_f32_e32 v215, v107
	v_exp_f32_e32 v107, v108
	v_exp_f32_e32 v217, v109
	v_exp_f32_e32 v166, v72
	v_exp_f32_e32 v96, v73
	v_exp_f32_e32 v168, v74
	v_exp_f32_e32 v98, v75
	v_exp_f32_e32 v210, v76
	v_exp_f32_e32 v100, v77
	v_exp_f32_e32 v212, v78
	v_exp_f32_e32 v102, v79
	v_exp_f32_e32 v214, v80
	v_exp_f32_e32 v104, v81
	s_waitcnt lgkmcnt(7)
	v_mfma_f32_32x32x16_f16 v[66:81], v[66:69], v[114:117], v[240:255]
	v_exp_f32_e32 v109, v110
	v_exp_f32_e32 v216, v82
	v_exp_f32_e32 v106, v83
	v_exp_f32_e32 v219, v111
	s_waitcnt lgkmcnt(6)
	v_mfma_f32_32x32x16_f16 v[66:81], v[158:161], v[118:121], v[66:81]
	v_exp_f32_e32 v218, v84
	v_exp_f32_e32 v108, v85
	v_exp_f32_e32 v111, v112
	v_exp_f32_e32 v110, v87
	s_waitcnt lgkmcnt(3)
	v_mfma_f32_32x32x16_f16 v[66:81], v[202:205], v[122:125], v[66:81]
	v_exp_f32_e32 v202, v86
	v_exp_f32_e32 v203, v113
	s_waitcnt lgkmcnt(2)
	v_mfma_f32_32x32x16_f16 v[66:81], v[206:209], v[126:129], v[66:81]
	s_waitcnt vmcnt(3)
	ds_write_b128 v185, v[88:91] offset:18432
	s_waitcnt vmcnt(2)
	ds_write_b128 v185, v[92:95] offset:27648
	s_waitcnt vmcnt(1)
	ds_write_b128 v185, v[150:153] offset:36864
	s_waitcnt vmcnt(0)
	ds_write_b128 v185, v[154:157] offset:46080
	v_fma_f32 v150, v176, v166, v97
	v_fma_f32 v151, v176, v96, v167
	v_mfma_f32_32x32x16_f16 v[82:97], v[194:197], v[130:133], 0
	v_fma_f32 v152, v176, v168, v99
	v_fma_f32 v153, v176, v98, v169
	v_fma_f32 v154, v176, v210, v101
	v_fma_f32 v155, v176, v100, v211
	v_fma_f32 v156, v176, v212, v103
	v_fma_f32 v157, v176, v102, v213
	v_fma_f32 v158, v176, v214, v105
	v_fma_f32 v159, v176, v104, v215
	v_fma_f32 v160, v176, v216, v107
	v_fma_f32 v161, v176, v106, v217
	v_fma_f32 v166, v176, v218, v109
	v_fma_f32 v167, v176, v108, v219
	v_fma_f32 v168, v176, v202, v111
	v_fma_f32 v169, v176, v110, v203
	ds_read_b128 v[98:101], v189
	ds_read_b128 v[102:105], v189 offset:1152
	ds_read_b128 v[106:109], v189 offset:2304
	ds_read_b128 v[110:113], v189 offset:3456
	ds_write_b128 v190, v[150:153]
	ds_write_b128 v190, v[154:157] offset:16
	ds_write_b128 v190, v[158:161] offset:64
	ds_write_b128 v190, v[166:169] offset:80
	v_cvt_pk_f16_f32 v157, v156, v157
	v_cvt_pk_f16_f32 v156, v154, v155
	v_cvt_pk_f16_f32 v155, v152, v153
	v_cvt_pk_f16_f32 v154, v150, v151
	ds_read_b128 v[150:153], v191 offset:55296
	ds_read_b128 v[194:197], v191 offset:55328
	v_mfma_f32_32x32x16_f16 v[82:97], v[198:201], v[134:137], v[82:97]
	s_and_b32 s2, s20, 0x7c0
	s_min_u32 s20, s19, 27
	s_lshl_b32 s2, s2, 2
	s_add_i32 s20, s18, s20
	v_lshl_add_u64 v[210:211], v[174:175], 0, s[2:3]
	s_lshl_b32 s2, s20, 13
	s_and_b32 s2, s2, 0x3e000
	s_waitcnt lgkmcnt(1)
	v_mfma_f32_32x32x16_f16 v[50:65], v[154:157], v[150:153], v[50:65]
	ds_read_b128 v[150:153], v191 offset:59904
	ds_read_b128 v[198:201], v191 offset:59936
	s_lshl_b32 s21, s21, 7
	v_cvt_pk_f16_f32 v169, v168, v169
	v_cvt_pk_f16_f32 v168, v166, v167
	v_cvt_pk_f16_f32 v166, v158, v159
	v_cvt_pk_f16_f32 v167, v160, v161
	s_addk_i32 s1, 0x80
	s_waitcnt lgkmcnt(1)
	v_mfma_f32_32x32x16_f16 v[34:49], v[154:157], v[150:153], v[34:49]
	ds_read_b128 v[150:153], v191 offset:64512
	ds_read_b128 v[202:205], v191 offset:64544
	s_waitcnt lgkmcnt(1)
	v_mfma_f32_32x32x16_f16 v[18:33], v[154:157], v[150:153], v[18:33]
	ds_read_b128 v[150:153], v192 offset:13824
	ds_read_b128 v[206:209], v192 offset:13856
	v_mfma_f32_32x32x16_f16 v[82:97], v[146:149], v[138:141], v[82:97]
	v_lshl_add_u64 v[146:147], v[170:171], 0, s[2:3]
	s_and_b32 s2, s21, 0xf80
	v_lshl_add_u64 v[158:159], v[172:173], 0, s[2:3]
	s_add_i32 s2, s19, 2
	s_cmp_lt_u32 s19, 30
	s_mov_b32 s19, s2
	s_waitcnt lgkmcnt(1)
	v_mfma_f32_32x32x16_f16 v[2:17], v[154:157], v[150:153], v[2:17]
	v_add_co_u32_e32 v150, vcc, s15, v146
	s_nop 1
	v_addc_co_u32_e32 v151, vcc, 0, v147, vcc
	global_load_dwordx4 v[146:149], v[146:147], off
	s_nop 0
	global_load_dwordx4 v[150:153], v[150:151], off
	s_nop 0
	global_load_dwordx4 v[154:157], v[158:159], off
	v_add_co_u32_e32 v158, vcc, s10, v158
	v_mfma_f32_32x32x16_f16 v[50:65], v[166:169], v[194:197], v[50:65]
	s_nop 0
	v_addc_co_u32_e32 v159, vcc, 0, v159, vcc
	global_load_dwordx4 v[158:161], v[158:159], off
	v_add_co_u32_e32 v194, vcc, s5, v210
	s_nop 1
	v_addc_co_u32_e32 v195, vcc, 0, v211, vcc
	v_mfma_f32_32x32x16_f16 v[34:49], v[166:169], v[198:201], v[34:49]
	v_add_co_u32_e32 v196, vcc, s13, v210
	s_nop 1
	v_addc_co_u32_e32 v197, vcc, 0, v211, vcc
	v_mfma_f32_32x32x16_f16 v[18:33], v[166:169], v[202:205], v[18:33]
	s_waitcnt lgkmcnt(0)
	v_mfma_f32_32x32x16_f16 v[2:17], v[166:169], v[206:209], v[2:17]
	v_add_co_u32_e32 v166, vcc, s14, v210
	s_nop 1
	v_addc_co_u32_e32 v167, vcc, 0, v211, vcc
	global_store_dwordx4 v[210:211], v[98:101], off nt
	global_store_dwordx4 v[194:195], v[102:105], off nt
	global_store_dwordx4 v[196:197], v[106:109], off nt
	global_store_dwordx4 v[166:167], v[110:113], off nt
	v_mfma_f32_32x32x16_f16 v[82:97], v[162:165], v[142:145], v[82:97]
	s_barrier
	s_cbranch_scc1 .Ll2f_top
